# v53 + sub-head-1 zero-start accumulators via MFMA C=0 with the 32 removed v_mov replaced by an equal idle spacer on that path (timing kept, VALU issue freed)
# speedup vs baseline: 1.0222x; 1.0027x over previous
.Lz_l1s1:
	s_nop 15
	s_nop 15
	v_add_u32_e32 v212, v0, v231
	v_add_u32_e32 v213, v0, v232
	v_add_u32_e32 v0, v0, v233
	s_waitcnt lgkmcnt(0)
	v_mfma_f32_32x32x16_bf16 v[160:175], v[248:251], v[192:195], 0
	ds_read_b128 v[248:251], v212 offset:8192
	v_mfma_f32_32x32x16_bf16 v[144:159], v[236:239], v[192:195], 0
	s_branch .Lc_l1s1

.LBB0_195:
	v_add_u32_e32 v0, s49, v225
	v_add_u32_e32 v6, v0, v227
	v_add_u32_e32 v7, v0, v228
	ds_read_b128 v[244:247], v6
	ds_read_b128 v[248:251], v6 offset:8192
	ds_read_b128 v[236:239], v7
	ds_read_b128 v[208:211], v7 offset:8192
	v_add_u32_e32 v6, v0, v229
	v_add_u32_e32 v7, v0, v230
	ds_read_b128 v[2:5], v6
	ds_read_b128 v[8:11], v6 offset:8192
	ds_read_b128 v[12:15], v7
	s_xor_b64 s[44:45], s[44:45], -1
	v_add_u32_e32 v6, v0, v226
	s_waitcnt lgkmcnt(6)
	v_mfma_f32_32x32x16_bf16 v[144:159], v[244:247], v[176:179], v[144:159]
	ds_read_b128 v[244:247], v7 offset:8192
	s_waitcnt lgkmcnt(6)
	v_mfma_f32_32x32x16_bf16 v[160:175], v[248:251], v[176:179], v[160:175]
	s_waitcnt lgkmcnt(5)
	v_mfma_f32_32x32x16_bf16 v[144:159], v[236:239], v[180:183], v[144:159]
	ds_read_b128 v[248:251], v6
	ds_read_b128 v[236:239], v6 offset:8192
	s_waitcnt lgkmcnt(6)
	v_mfma_f32_32x32x16_bf16 v[160:175], v[208:211], v[180:183], v[160:175]
	v_add_u32_e32 v7, v0, v231
	s_waitcnt lgkmcnt(5)
	v_mfma_f32_32x32x16_bf16 v[144:159], v[2:5], v[184:187], v[144:159]
	s_waitcnt lgkmcnt(4)
	v_mfma_f32_32x32x16_bf16 v[160:175], v[8:11], v[184:187], v[160:175]
	s_waitcnt lgkmcnt(3)
	v_mfma_f32_32x32x16_bf16 v[144:159], v[12:15], v[188:191], v[144:159]
	s_waitcnt lgkmcnt(2)
	v_mfma_f32_32x32x16_bf16 v[160:175], v[244:247], v[188:191], v[160:175]
	ds_read_b128 v[244:247], v7
	s_nop 9
	v_exp_f32_e32 v6, v144
	v_exp_f32_e32 v3, v145
	v_exp_f32_e32 v10, v148
	v_exp_f32_e32 v11, v149
	v_exp_f32_e32 v12, v150
	v_exp_f32_e32 v148, v152
	v_exp_f32_e32 v150, v153
	v_exp_f32_e32 v156, v156
	v_exp_f32_e32 v157, v157
	v_exp_f32_e32 v5, v146
	v_exp_f32_e32 v152, v154
	v_exp_f32_e32 v158, v158
	v_exp_f32_e32 v8, v147
	v_exp_f32_e32 v13, v151
	v_exp_f32_e32 v154, v155
	v_exp_f32_e32 v159, v159
	v_exp_f32_e32 v2, v160
	v_exp_f32_e32 v144, v164
	v_exp_f32_e32 v149, v168
	v_exp_f32_e32 v160, v172
	v_exp_f32_e32 v4, v161
	v_exp_f32_e32 v145, v165
	v_exp_f32_e32 v151, v169
	v_exp_f32_e32 v161, v173
	v_add_f32_e32 v14, v6, v3
	v_add_f32_e32 v15, v10, v11
	v_add_f32_e32 v164, v148, v150
	v_add_f32_e32 v165, v156, v157
	v_exp_f32_e32 v7, v162
	v_exp_f32_e32 v146, v166
	v_exp_f32_e32 v153, v170
	v_exp_f32_e32 v162, v174
	v_add_f32_e32 v14, v5, v14
	v_add_f32_e32 v15, v12, v15
	v_add_f32_e32 v164, v152, v164
	v_add_f32_e32 v165, v158, v165
	v_exp_f32_e32 v9, v163
	v_exp_f32_e32 v147, v167
	v_exp_f32_e32 v155, v171
	v_exp_f32_e32 v163, v175
	v_add_f32_e32 v14, v8, v14
	v_add_f32_e32 v15, v13, v15
	v_add_f32_e32 v164, v154, v164
	v_add_f32_e32 v165, v159, v165
	v_add_f32_e32 v14, v2, v14
	v_add_f32_e32 v15, v144, v15
	v_add_f32_e32 v164, v149, v164
	v_add_f32_e32 v165, v160, v165
	v_add_f32_e32 v14, v4, v14
	v_add_f32_e32 v15, v145, v15
	v_add_f32_e32 v164, v151, v164
	v_add_f32_e32 v165, v161, v165
	v_add_f32_e32 v14, v7, v14
	v_add_f32_e32 v15, v146, v15
	v_add_f32_e32 v164, v153, v164
	v_add_f32_e32 v165, v162, v165
	v_add_f32_e32 v14, v9, v14
	v_add_f32_e32 v15, v147, v15
	v_add_f32_e32 v164, v155, v164
	v_add_f32_e32 v165, v163, v165
	v_add_f32_e32 v14, v14, v15
	v_add_f32_e32 v15, v164, v165
	v_add_f32_e32 v14, v14, v15
	v_mov_b32_e32 v15, v14
	v_cvt_pk_bf16_f32 v208, v6, v3
	v_cvt_pk_bf16_f32 v209, v5, v8
	v_cvt_pk_bf16_f32 v210, v10, v11
	v_cvt_pk_bf16_f32 v211, v12, v13
	v_cvt_pk_bf16_f32 v10, v148, v150
	v_cvt_pk_bf16_f32 v11, v152, v154
	v_cvt_pk_bf16_f32 v12, v156, v157
	v_cvt_pk_bf16_f32 v13, v158, v159
	v_cvt_pk_bf16_f32 v6, v2, v4
	v_cvt_pk_bf16_f32 v7, v7, v9
	v_cvt_pk_bf16_f32 v8, v144, v145
	v_cvt_pk_bf16_f32 v9, v146, v147
	v_cvt_pk_bf16_f32 v2, v149, v151
	v_cvt_pk_bf16_f32 v3, v153, v155
	v_cvt_pk_bf16_f32 v4, v160, v161
	v_cvt_pk_bf16_f32 v5, v162, v163
	v_permlane32_swap_b32_e32 v14, v15
	v_permlane32_swap_b32_e32 v208, v210
	v_permlane32_swap_b32_e32 v209, v211
	v_permlane32_swap_b32_e32 v10, v12
	v_permlane32_swap_b32_e32 v11, v13
	v_permlane32_swap_b32_e32 v6, v8
	v_permlane32_swap_b32_e32 v7, v9
	v_permlane32_swap_b32_e32 v2, v4
	v_permlane32_swap_b32_e32 v3, v5
	s_nop 15
	s_nop 15
	s_andn2_b64 vcc, exec, s[44:45]
	s_cbranch_vccnz .Lz_l1s1
	s_andn2_b64 vcc, exec, s[42:43]
	s_mov_b64 s[42:43], -1
	s_cbranch_vccnz .LBB0_198
	v_add_u32_e32 v144, 0x21780, v212
	v_add_u32_e32 v146, 0x21708, v212
	v_add_u32_e32 v147, 0x21788, v212
	v_add_u32_e32 v148, 0x21720, v212
	v_add_u32_e32 v149, 0x217a0, v212
	v_add_u32_e32 v150, 0x21728, v212
	v_add_u32_e32 v151, 0x217a8, v212
	v_add_u32_e32 v152, 0x21740, v212
	v_add_u32_e32 v153, 0x217c0, v212
	v_add_u32_e32 v154, 0x21748, v212
	v_add_u32_e32 v155, 0x217c8, v212
	v_add_u32_e32 v156, 0x21760, v212
	v_add_u32_e32 v157, 0x217e0, v212
	v_add_u32_e32 v158, 0x21768, v212
	v_add_u32_e32 v159, 0x217e8, v212
	ds_read2_b32 v[160:161], v213 offset1:1
	ds_read2_b32 v[144:145], v144 offset1:1
	ds_read2_b32 v[162:163], v146 offset1:1
	ds_read2_b32 v[146:147], v147 offset1:1
	ds_read2_b32 v[164:165], v148 offset1:1
	ds_read2_b32 v[148:149], v149 offset1:1
	ds_read2_b32 v[166:167], v150 offset1:1
	ds_read2_b32 v[150:151], v151 offset1:1
	ds_read2_b32 v[168:169], v152 offset1:1
	ds_read2_b32 v[152:153], v153 offset1:1
	ds_read2_b32 v[170:171], v154 offset1:1
	ds_read2_b32 v[154:155], v155 offset1:1
	ds_read2_b32 v[172:173], v156 offset1:1
	ds_read2_b32 v[156:157], v157 offset1:1
	ds_read2_b32 v[174:175], v158 offset1:1
	ds_read2_b32 v[158:159], v159 offset1:1
	s_mov_b64 s[42:43], 0

.Lc_l1s1:
	ds_read_b128 v[236:239], v213
	v_mfma_f32_32x32x16_bf16 v[160:175], v[244:247], v[196:199], v[160:175]
	ds_read_b128 v[244:247], v213 offset:8192
	s_waitcnt lgkmcnt(2)
	v_mfma_f32_32x32x16_bf16 v[144:159], v[248:251], v[196:199], v[144:159]
	ds_read_b128 v[248:251], v0
	s_waitcnt lgkmcnt(2)
	v_mfma_f32_32x32x16_bf16 v[160:175], v[236:239], v[200:203], v[160:175]
	ds_read_b128 v[236:239], v0 offset:8192
	s_waitcnt lgkmcnt(2)
	v_mfma_f32_32x32x16_bf16 v[144:159], v[244:247], v[200:203], v[144:159]
	v_add_f32_e32 v0, v14, v15
	v_add_f32_e32 v235, v235, v0
	s_waitcnt lgkmcnt(1)
	v_mfma_f32_32x32x16_bf16 v[160:175], v[248:251], v[204:207], v[160:175]
	s_waitcnt lgkmcnt(0)
	v_mfma_f32_32x32x16_bf16 v[144:159], v[236:239], v[204:207], v[144:159]
	s_nop 10
	v_exp_f32_e32 v14, v160
	v_exp_f32_e32 v160, v161
	v_exp_f32_e32 v164, v164
	v_exp_f32_e32 v15, v168
	v_exp_f32_e32 v161, v169
	v_exp_f32_e32 v162, v162
	v_exp_f32_e32 v220, v163
	v_exp_f32_e32 v166, v166
	s_nop 4
	v_exp_f32_e32 v246, v148
	v_exp_f32_e32 v148, v165
	v_exp_f32_e32 v248, v149
	v_exp_f32_e32 v165, v172
	v_exp_f32_e32 v149, v173
	v_exp_f32_e32 v250, v150
	v_exp_f32_e32 v150, v167
	v_exp_f32_e32 v163, v170
	v_exp_f32_e32 v167, v174
	v_exp_f32_e32 v252, v151
	v_exp_f32_e32 v221, v171
	v_exp_f32_e32 v151, v175
	v_exp_f32_e32 v144, v144
	v_exp_f32_e32 v212, v145
	v_exp_f32_e32 v145, v152
	v_exp_f32_e32 v247, v156
	v_exp_f32_e32 v244, v147
	v_exp_f32_e32 v213, v153
	v_exp_f32_e32 v147, v154
	v_exp_f32_e32 v245, v155
	v_exp_f32_e32 v249, v157
	v_add_f32_e32 v152, v14, v160
	v_add_f32_e32 v153, v15, v161
	v_add_f32_e32 v154, v164, v148
	v_add_f32_e32 v155, v165, v149
	v_exp_f32_e32 v146, v146
	v_exp_f32_e32 v251, v158
	v_add_f32_e32 v152, v162, v152
	v_add_f32_e32 v153, v163, v153
	v_add_f32_e32 v154, v166, v154
	v_add_f32_e32 v155, v167, v155
	v_exp_f32_e32 v253, v159
	v_add_f32_e32 v152, v220, v152
	v_add_f32_e32 v153, v221, v153
	v_add_f32_e32 v154, v150, v154
	v_add_f32_e32 v155, v151, v155
	v_add_f32_e32 v152, v144, v152
	v_add_f32_e32 v153, v145, v153
	v_add_f32_e32 v154, v246, v154
	v_add_f32_e32 v155, v247, v155
	v_add_f32_e32 v152, v212, v152
	v_add_f32_e32 v153, v213, v153
	v_add_f32_e32 v154, v248, v154
	v_add_f32_e32 v155, v249, v155
	v_add_f32_e32 v152, v146, v152
	v_add_f32_e32 v153, v147, v153
	v_add_f32_e32 v154, v250, v154
	v_add_f32_e32 v155, v251, v155
	v_add_f32_e32 v152, v244, v152
	v_add_f32_e32 v153, v245, v153
	v_add_f32_e32 v154, v252, v154
	v_add_f32_e32 v155, v253, v155
	v_cvt_pk_bf16_f32 v156, v14, v160
	v_add_f32_e32 v152, v152, v154
	v_add_f32_e32 v153, v153, v155
	v_cvt_pk_bf16_f32 v157, v162, v220
	v_add_f32_e32 v152, v152, v153
	v_mov_b32_e32 v153, v152
	v_cvt_pk_bf16_f32 v158, v164, v148
	v_mov_b32_e32 v0, v152
	s_nop 1
	v_permlane32_swap_b32_e32 v152, v0
	v_add_f32_e32 v0, v152, v0
	v_cvt_pk_bf16_f32 v159, v166, v150
	v_cvt_pk_bf16_f32 v152, v15, v161
	v_cvt_pk_bf16_f32 v153, v163, v221
	v_cvt_pk_bf16_f32 v154, v165, v149
	v_cvt_pk_bf16_f32 v155, v167, v151
	v_cvt_pk_bf16_f32 v148, v144, v212
	v_cvt_pk_bf16_f32 v149, v146, v244
	v_cvt_pk_bf16_f32 v150, v246, v248
	v_cvt_pk_bf16_f32 v151, v250, v252
	v_cvt_pk_bf16_f32 v144, v145, v213
	v_cvt_pk_bf16_f32 v145, v147, v245
	v_cvt_pk_bf16_f32 v146, v247, v249
	v_cvt_pk_bf16_f32 v147, v251, v253
	v_add_f32_e32 v234, v234, v0
	v_permlane32_swap_b32_e32 v156, v158
	v_permlane32_swap_b32_e32 v157, v159
	v_permlane32_swap_b32_e32 v152, v154
	v_permlane32_swap_b32_e32 v153, v155
	v_permlane32_swap_b32_e32 v148, v150
	v_permlane32_swap_b32_e32 v149, v151
	v_permlane32_swap_b32_e32 v144, v146
	v_permlane32_swap_b32_e32 v145, v147
	s_add_i32 s42, s49, 0x4000
	s_cmpk_lg_u32 s49, 0xc000
	s_cselect_b32 s42, s42, 0
	s_add_i32 s43, s90, 0x4000
	s_cmpk_lg_u32 s90, 0xc000
	s_cselect_b32 s90, s43, 0
	s_add_u32 s40, s40, 0x60000
	s_addc_u32 s41, s41, 0
	s_addk_i32 s71, 0x100
	s_add_i32 s73, s73, 64
	s_add_i32 s86, s86, 1
	s_cmpk_eq_i32 s71, 0x4000
	s_cbranch_scc1 .LBB0_202
	s_mov_b32 s44, s49
	s_mov_b32 s49, s42
	s_cmpk_eq_i32 s71, 0x3f00
	s_mov_b64 s[42:43], -1
	s_cbranch_scc0 .LBB0_191
	s_branch .LBB0_185

.Lc_l2s1:
	ds_read_b128 v[236:239], v219 offset:8192
	v_mfma_f32_32x32x16_bf16 v[144:159], v[240:243], v[196:199], v[144:159]
	ds_read_b128 v[240:243], v212
	v_mfma_f32_32x32x16_bf16 v[160:175], v[244:247], v[196:199], v[160:175]
	ds_read_b128 v[244:247], v212 offset:8192
	s_waitcnt lgkmcnt(3)
	v_mfma_f32_32x32x16_bf16 v[144:159], v[248:251], v[200:203], v[144:159]
	s_waitcnt lgkmcnt(2)
	v_mfma_f32_32x32x16_bf16 v[160:175], v[236:239], v[200:203], v[160:175]
	v_add_f32_e32 v212, v213, v218
	v_add_f32_e32 v235, v235, v212
	s_waitcnt lgkmcnt(1)
	v_mfma_f32_32x32x16_bf16 v[144:159], v[240:243], v[204:207], v[144:159]
	s_waitcnt lgkmcnt(0)
	v_mfma_f32_32x32x16_bf16 v[160:175], v[244:247], v[204:207], v[160:175]
	s_nop 10
	v_exp_f32_e32 v212, v144
	v_exp_f32_e32 v218, v145
	v_exp_f32_e32 v242, v148
	v_exp_f32_e32 v244, v149
	v_exp_f32_e32 v213, v152
	v_exp_f32_e32 v219, v153
	v_exp_f32_e32 v243, v156
	v_exp_f32_e32 v245, v157
	v_exp_f32_e32 v236, v146
	v_exp_f32_e32 v150, v150
	v_exp_f32_e32 v248, v151
	v_exp_f32_e32 v237, v154
	v_exp_f32_e32 v151, v158
	v_exp_f32_e32 v238, v147
	v_exp_f32_e32 v239, v155
	v_exp_f32_e32 v249, v159
	v_exp_f32_e32 v160, v160
	v_exp_f32_e32 v220, v161
	v_exp_f32_e32 v164, v164
	v_exp_f32_e32 v246, v165
	v_exp_f32_e32 v161, v168
	v_exp_f32_e32 v165, v172
	v_exp_f32_e32 v221, v169
	v_exp_f32_e32 v247, v173
	v_add_f32_e32 v144, v212, v218
	v_add_f32_e32 v145, v213, v219
	v_add_f32_e32 v146, v242, v244
	v_add_f32_e32 v147, v243, v245
	v_exp_f32_e32 v162, v162
	v_exp_f32_e32 v240, v163
	v_exp_f32_e32 v166, v166
	v_exp_f32_e32 v250, v167
	v_exp_f32_e32 v163, v170
	v_exp_f32_e32 v167, v174
	v_add_f32_e32 v144, v236, v144
	v_add_f32_e32 v145, v237, v145
	v_add_f32_e32 v146, v150, v146
	v_add_f32_e32 v147, v151, v147
	v_exp_f32_e32 v241, v171
	v_exp_f32_e32 v251, v175
	v_add_f32_e32 v144, v238, v144
	v_add_f32_e32 v145, v239, v145
	v_add_f32_e32 v146, v248, v146
	v_add_f32_e32 v147, v249, v147
	v_add_f32_e32 v144, v160, v144
	v_add_f32_e32 v145, v161, v145
	v_add_f32_e32 v146, v164, v146
	v_add_f32_e32 v147, v165, v147
	v_add_f32_e32 v144, v220, v144
	v_add_f32_e32 v145, v221, v145
	v_add_f32_e32 v146, v246, v146
	v_add_f32_e32 v147, v247, v147
	v_add_f32_e32 v144, v162, v144
	v_add_f32_e32 v145, v163, v145
	v_add_f32_e32 v146, v166, v146
	v_add_f32_e32 v147, v167, v147
	v_add_f32_e32 v144, v240, v144
	v_add_f32_e32 v145, v241, v145
	v_add_f32_e32 v146, v250, v146
	v_add_f32_e32 v147, v251, v147
	v_cvt_pk_bf16_f32 v148, v213, v219
	v_add_f32_e32 v144, v144, v146
	v_add_f32_e32 v145, v145, v147
	v_cvt_pk_bf16_f32 v146, v242, v244
	v_add_f32_e32 v144, v144, v145
	v_mov_b32_e32 v145, v144
	v_cvt_pk_bf16_f32 v147, v150, v248
	v_mov_b32_e32 v145, v144
	s_nop 1
	v_permlane32_swap_b32_e32 v144, v145
	v_add_f32_e32 v144, v144, v145
	v_add_f32_e32 v234, v234, v144
	v_cvt_pk_bf16_f32 v144, v212, v218
	v_cvt_pk_bf16_f32 v145, v236, v238
	v_cvt_pk_bf16_f32 v149, v237, v239
	v_cvt_pk_bf16_f32 v150, v243, v245
	v_cvt_pk_bf16_f32 v151, v151, v249
	v_cvt_pk_bf16_f32 v152, v160, v220
	v_cvt_pk_bf16_f32 v153, v162, v240
	v_cvt_pk_bf16_f32 v154, v164, v246
	v_cvt_pk_bf16_f32 v155, v166, v250
	v_cvt_pk_bf16_f32 v156, v161, v221
	v_cvt_pk_bf16_f32 v157, v163, v241
	v_cvt_pk_bf16_f32 v158, v165, v247
	v_cvt_pk_bf16_f32 v159, v167, v251
	v_permlane32_swap_b32_e32 v144, v146
	v_permlane32_swap_b32_e32 v145, v147
	v_permlane32_swap_b32_e32 v148, v150
	v_permlane32_swap_b32_e32 v149, v151
	v_permlane32_swap_b32_e32 v152, v154
	v_permlane32_swap_b32_e32 v153, v155
	v_permlane32_swap_b32_e32 v156, v158
	v_permlane32_swap_b32_e32 v157, v159
	s_waitcnt lgkmcnt(0)
	v_add_u32_e32 v212, s56, v224
	ds_read_b64_tr_b16 v[160:161], v212 offset:0
	ds_read_b64_tr_b16 v[162:163], v212 offset:0x800
	ds_read_b64_tr_b16 v[164:165], v212 offset:0x200
	ds_read_b64_tr_b16 v[166:167], v212 offset:0xa00
	ds_read_b64_tr_b16 v[168:169], v212 offset:0x400
	ds_read_b64_tr_b16 v[170:171], v212 offset:0xc00
	ds_read_b64_tr_b16 v[172:173], v212 offset:0x600
	ds_read_b64_tr_b16 v[174:175], v212 offset:0xe00
	s_waitcnt lgkmcnt(4)
	s_nop 0
	v_mfma_f32_32x32x16_bf16 v[112:127], v[208:211], v[160:163], v[112:127]
	v_mfma_f32_32x32x16_bf16 v[96:111], v[208:211], v[164:167], v[96:111]
	v_mfma_f32_32x32x16_bf16 v[128:143], v[144:147], v[160:163], v[128:143]
	v_mfma_f32_32x32x16_bf16 v[80:95], v[144:147], v[164:167], v[80:95]
	ds_read_b64_tr_b16 v[160:161], v212 offset:0x1000
	ds_read_b64_tr_b16 v[162:163], v212 offset:0x1800
	ds_read_b64_tr_b16 v[164:165], v212 offset:0x1200
	ds_read_b64_tr_b16 v[166:167], v212 offset:0x1a00
	s_waitcnt lgkmcnt(4)
	v_mfma_f32_32x32x16_bf16 v[64:79], v[208:211], v[168:171], v[64:79]
	v_mfma_f32_32x32x16_bf16 v[48:63], v[208:211], v[172:175], v[48:63]
	v_mfma_f32_32x32x16_bf16 v[32:47], v[144:147], v[168:171], v[32:47]
	v_mfma_f32_32x32x16_bf16 v[16:31], v[144:147], v[172:175], v[16:31]
	ds_read_b64_tr_b16 v[144:145], v212 offset:0x1400
	ds_read_b64_tr_b16 v[146:147], v212 offset:0x1c00
	ds_read_b64_tr_b16 v[168:169], v212 offset:0x1600
	ds_read_b64_tr_b16 v[170:171], v212 offset:0x1e00
	s_waitcnt lgkmcnt(4)
	v_mfma_f32_32x32x16_bf16 v[112:127], v[10:13], v[160:163], v[112:127]
	v_mfma_f32_32x32x16_bf16 v[96:111], v[10:13], v[164:167], v[96:111]
	v_mfma_f32_32x32x16_bf16 v[128:143], v[148:151], v[160:163], v[128:143]
	v_mfma_f32_32x32x16_bf16 v[80:95], v[148:151], v[164:167], v[80:95]
	ds_read_b64_tr_b16 v[160:161], v212 offset:0x2000
	ds_read_b64_tr_b16 v[162:163], v212 offset:0x2800
	ds_read_b64_tr_b16 v[164:165], v212 offset:0x2200
	ds_read_b64_tr_b16 v[166:167], v212 offset:0x2a00
	s_waitcnt lgkmcnt(4)
	v_mfma_f32_32x32x16_bf16 v[64:79], v[10:13], v[144:147], v[64:79]
	v_mfma_f32_32x32x16_bf16 v[48:63], v[10:13], v[168:171], v[48:63]
	v_mfma_f32_32x32x16_bf16 v[32:47], v[148:151], v[144:147], v[32:47]
	v_mfma_f32_32x32x16_bf16 v[16:31], v[148:151], v[168:171], v[16:31]
	ds_read_b64_tr_b16 v[10:11], v212 offset:0x2400
	ds_read_b64_tr_b16 v[12:13], v212 offset:0x2c00
	ds_read_b64_tr_b16 v[144:145], v212 offset:0x2600
	ds_read_b64_tr_b16 v[146:147], v212 offset:0x2e00
	s_waitcnt lgkmcnt(4)
	v_mfma_f32_32x32x16_bf16 v[112:127], v[6:9], v[160:163], v[112:127]
	v_mfma_f32_32x32x16_bf16 v[96:111], v[6:9], v[164:167], v[96:111]
	v_mfma_f32_32x32x16_bf16 v[128:143], v[152:155], v[160:163], v[128:143]
	v_mfma_f32_32x32x16_bf16 v[80:95], v[152:155], v[164:167], v[80:95]
	ds_read_b64_tr_b16 v[148:149], v212 offset:0x3000
	ds_read_b64_tr_b16 v[150:151], v212 offset:0x3800
	ds_read_b64_tr_b16 v[160:161], v212 offset:0x3200
	ds_read_b64_tr_b16 v[162:163], v212 offset:0x3a00
	s_waitcnt lgkmcnt(4)
	v_mfma_f32_32x32x16_bf16 v[64:79], v[6:9], v[10:13], v[64:79]
	v_mfma_f32_32x32x16_bf16 v[48:63], v[6:9], v[144:147], v[48:63]
	v_mfma_f32_32x32x16_bf16 v[32:47], v[152:155], v[10:13], v[32:47]
	v_mfma_f32_32x32x16_bf16 v[16:31], v[152:155], v[144:147], v[16:31]
	ds_read_b64_tr_b16 v[6:7], v212 offset:0x3400
	ds_read_b64_tr_b16 v[8:9], v212 offset:0x3c00
	ds_read_b64_tr_b16 v[10:11], v212 offset:0x3600
	ds_read_b64_tr_b16 v[12:13], v212 offset:0x3e00
	s_waitcnt lgkmcnt(4)
	v_mfma_f32_32x32x16_bf16 v[112:127], v[2:5], v[148:151], v[112:127]
	v_mfma_f32_32x32x16_bf16 v[96:111], v[2:5], v[160:163], v[96:111]
	v_mfma_f32_32x32x16_bf16 v[128:143], v[156:159], v[148:151], v[128:143]
	v_mfma_f32_32x32x16_bf16 v[80:95], v[156:159], v[160:163], v[80:95]
	s_waitcnt lgkmcnt(0)
	v_mfma_f32_32x32x16_bf16 v[64:79], v[2:5], v[6:9], v[64:79]
	v_mfma_f32_32x32x16_bf16 v[48:63], v[2:5], v[10:13], v[48:63]
	v_mfma_f32_32x32x16_bf16 v[32:47], v[156:159], v[6:9], v[32:47]
	v_mfma_f32_32x32x16_bf16 v[16:31], v[156:159], v[10:13], v[16:31]
	s_add_i32 s42, s56, 0x4000
	s_cmpk_lg_u32 s56, 0xc000
	s_cselect_b32 s56, s42, 0
	s_add_i32 s42, s90, 0x4000
	s_cmpk_lg_u32 s90, 0xc000
	s_cselect_b32 s90, s42, 0
	s_add_u32 s40, s40, 0x60000
	s_addc_u32 s41, s41, 0
	s_addk_i32 s73, 0x100
	s_add_i32 s72, s72, 64
	s_add_i32 s71, s71, 1
	s_cmpk_eq_i32 s73, 0x4000
	s_cbranch_scc1 .LBB0_220

.Lz_l2s1:
	s_nop 15
	s_nop 15
	v_add_u32_e32 v219, v212, v232
	v_add_u32_e32 v212, v212, v233
	s_waitcnt lgkmcnt(0)
	v_mfma_f32_32x32x16_bf16 v[144:159], v[248:251], v[192:195], 0
	ds_read_b128 v[248:251], v219
	v_mfma_f32_32x32x16_bf16 v[160:175], v[236:239], v[192:195], 0
	s_branch .Lc_l2s1

.LBB0_215:
	v_add_u32_e32 v212, s56, v225
	v_add_u32_e32 v6, v212, v227
	v_add_u32_e32 v7, v212, v228
	ds_read_b128 v[244:247], v6
	ds_read_b128 v[248:251], v6 offset:8192
	ds_read_b128 v[236:239], v7
	ds_read_b128 v[240:243], v7 offset:8192
	v_add_u32_e32 v6, v212, v229
	v_add_u32_e32 v7, v212, v230
	ds_read_b128 v[2:5], v6
	ds_read_b128 v[8:11], v6 offset:8192
	ds_read_b128 v[208:211], v7
	s_xor_b64 s[44:45], s[44:45], -1
	v_add_u32_e32 v6, v212, v226
	s_waitcnt lgkmcnt(6)
	v_mfma_f32_32x32x16_bf16 v[160:175], v[244:247], v[176:179], v[160:175]
	ds_read_b128 v[244:247], v7 offset:8192
	s_waitcnt lgkmcnt(6)
	v_mfma_f32_32x32x16_bf16 v[144:159], v[248:251], v[176:179], v[144:159]
	s_waitcnt lgkmcnt(5)
	v_mfma_f32_32x32x16_bf16 v[160:175], v[236:239], v[180:183], v[160:175]
	v_add_u32_e32 v7, v212, v231
	s_waitcnt lgkmcnt(4)
	v_mfma_f32_32x32x16_bf16 v[144:159], v[240:243], v[180:183], v[144:159]
	ds_read_b128 v[248:251], v6
	ds_read_b128 v[236:239], v6 offset:8192
	ds_read_b128 v[240:243], v7
	s_waitcnt lgkmcnt(6)
	v_mfma_f32_32x32x16_bf16 v[160:175], v[2:5], v[184:187], v[160:175]
	s_waitcnt lgkmcnt(5)
	v_mfma_f32_32x32x16_bf16 v[144:159], v[8:11], v[184:187], v[144:159]
	s_waitcnt lgkmcnt(4)
	v_mfma_f32_32x32x16_bf16 v[160:175], v[208:211], v[188:191], v[160:175]
	s_waitcnt lgkmcnt(3)
	v_mfma_f32_32x32x16_bf16 v[144:159], v[244:247], v[188:191], v[144:159]
	ds_read_b128 v[244:247], v7 offset:8192
	s_nop 9
	v_exp_f32_e32 v6, v160
	v_exp_f32_e32 v3, v161
	v_exp_f32_e32 v10, v164
	v_exp_f32_e32 v11, v165
	v_exp_f32_e32 v160, v172
	v_exp_f32_e32 v161, v173
	v_exp_f32_e32 v5, v162
	v_exp_f32_e32 v2, v144
	v_exp_f32_e32 v7, v146
	v_exp_f32_e32 v144, v148
	v_exp_f32_e32 v146, v150
	v_exp_f32_e32 v148, v168
	v_exp_f32_e32 v150, v169
	v_exp_f32_e32 v4, v145
	v_exp_f32_e32 v145, v149
	v_exp_f32_e32 v12, v166
	v_exp_f32_e32 v149, v152
	v_exp_f32_e32 v152, v170
	v_exp_f32_e32 v162, v174
	v_exp_f32_e32 v8, v163
	v_exp_f32_e32 v9, v147
	v_exp_f32_e32 v13, v167
	v_exp_f32_e32 v147, v151
	v_exp_f32_e32 v151, v153
	v_exp_f32_e32 v153, v154
	v_exp_f32_e32 v154, v171
	v_exp_f32_e32 v163, v175
	v_exp_f32_e32 v156, v156
	v_exp_f32_e32 v157, v157
	v_add_f32_e32 v164, v6, v3
	v_add_f32_e32 v165, v10, v11
	v_add_f32_e32 v166, v148, v150
	v_add_f32_e32 v167, v160, v161
	v_exp_f32_e32 v158, v158
	v_add_f32_e32 v164, v5, v164
	v_add_f32_e32 v165, v12, v165
	v_add_f32_e32 v166, v152, v166
	v_add_f32_e32 v167, v162, v167
	v_exp_f32_e32 v155, v155
	v_exp_f32_e32 v159, v159
	v_add_f32_e32 v164, v8, v164
	v_add_f32_e32 v165, v13, v165
	v_add_f32_e32 v166, v154, v166
	v_add_f32_e32 v167, v163, v167
	v_add_f32_e32 v164, v2, v164
	v_add_f32_e32 v165, v144, v165
	v_add_f32_e32 v166, v149, v166
	v_add_f32_e32 v167, v156, v167
	v_add_f32_e32 v164, v4, v164
	v_add_f32_e32 v165, v145, v165
	v_add_f32_e32 v166, v151, v166
	v_add_f32_e32 v167, v157, v167
	v_add_f32_e32 v164, v7, v164
	v_add_f32_e32 v165, v146, v165
	v_add_f32_e32 v166, v153, v166
	v_add_f32_e32 v167, v158, v167
	v_add_f32_e32 v164, v9, v164
	v_add_f32_e32 v165, v147, v165
	v_add_f32_e32 v166, v155, v166
	v_add_f32_e32 v167, v159, v167
	v_add_f32_e32 v164, v164, v165
	v_add_f32_e32 v165, v166, v167
	v_add_f32_e32 v213, v164, v165
	v_mov_b32_e32 v218, v213
	v_cvt_pk_bf16_f32 v208, v6, v3
	v_cvt_pk_bf16_f32 v209, v5, v8
	v_cvt_pk_bf16_f32 v210, v10, v11
	v_cvt_pk_bf16_f32 v211, v12, v13
	v_cvt_pk_bf16_f32 v10, v148, v150
	v_cvt_pk_bf16_f32 v11, v152, v154
	v_cvt_pk_bf16_f32 v12, v160, v161
	v_cvt_pk_bf16_f32 v13, v162, v163
	v_cvt_pk_bf16_f32 v6, v2, v4
	v_cvt_pk_bf16_f32 v7, v7, v9
	v_cvt_pk_bf16_f32 v8, v144, v145
	v_cvt_pk_bf16_f32 v9, v146, v147
	v_cvt_pk_bf16_f32 v2, v149, v151
	v_cvt_pk_bf16_f32 v3, v153, v155
	v_cvt_pk_bf16_f32 v4, v156, v157
	v_cvt_pk_bf16_f32 v5, v158, v159
	v_permlane32_swap_b32_e32 v213, v218
	v_permlane32_swap_b32_e32 v208, v210
	v_permlane32_swap_b32_e32 v209, v211
	v_permlane32_swap_b32_e32 v10, v12
	v_permlane32_swap_b32_e32 v11, v13
	v_permlane32_swap_b32_e32 v6, v8
	v_permlane32_swap_b32_e32 v7, v9
	v_permlane32_swap_b32_e32 v2, v4
	v_permlane32_swap_b32_e32 v3, v5
	s_nop 15
	s_nop 15
	s_andn2_b64 vcc, exec, s[44:45]
	s_cbranch_vccnz .Lz_l2s1
	s_andn2_b64 vcc, exec, s[42:43]
	s_mov_b64 s[42:43], -1
	s_cbranch_vccnz .LBB0_218
	v_add_u32_e32 v146, 0x21780, v219
	v_add_u32_e32 v147, 0x21708, v219
	v_add_u32_e32 v148, 0x21788, v219
	ds_read2_b32 v[144:145], v220 offset1:1
	ds_read2_b32 v[160:161], v146 offset1:1
	ds_read2_b32 v[146:147], v147 offset1:1
	ds_read2_b32 v[162:163], v148 offset1:1
	v_add_u32_e32 v148, 0x21720, v219
	v_add_u32_e32 v150, 0x217a0, v219
	v_add_u32_e32 v151, 0x21728, v219
	v_add_u32_e32 v152, 0x217a8, v219
	ds_read2_b32 v[148:149], v148 offset1:1
	ds_read2_b32 v[164:165], v150 offset1:1
	ds_read2_b32 v[150:151], v151 offset1:1
	ds_read2_b32 v[166:167], v152 offset1:1
	v_add_u32_e32 v152, 0x21740, v219
	v_add_u32_e32 v154, 0x217c0, v219
	v_add_u32_e32 v155, 0x21748, v219
	v_add_u32_e32 v156, 0x217c8, v219
	ds_read2_b32 v[152:153], v152 offset1:1
	ds_read2_b32 v[168:169], v154 offset1:1
	ds_read2_b32 v[154:155], v155 offset1:1
	ds_read2_b32 v[170:171], v156 offset1:1
	v_add_u32_e32 v156, 0x21760, v219
	v_add_u32_e32 v158, 0x217e0, v219
	v_add_u32_e32 v159, 0x21768, v219
	v_add_u32_e32 v174, 0x217e8, v219
	ds_read2_b32 v[156:157], v156 offset1:1
	ds_read2_b32 v[172:173], v158 offset1:1
	ds_read2_b32 v[158:159], v159 offset1:1
	ds_read2_b32 v[174:175], v174 offset1:1
	s_mov_b64 s[42:43], 0
